# baseline (speedup 1.0000x reference)
.LBB3_2:
	v_add_u32_e32 v206, s27, v214
	ds_read_b64_tr_b16 v[194:195], v206 offset:24576
	ds_read_b64_tr_b16 v[196:197], v206 offset:25088
	s_waitcnt lgkmcnt(9)
	v_mfma_f32_32x32x16_bf16 v[114:129], v[190:193], v[158:161], v[50:65]
	v_add_f32_e32 v98, v82, v83
	v_add_f32_e32 v98, v84, v98
	v_add_f32_e32 v98, v85, v98
	v_add_f32_e32 v98, v86, v98
	v_add_f32_e32 v130, v87, v98
	v_cvt_pk_bf16_f32 v142, v82, v83
	v_cvt_pk_bf16_f32 v143, v84, v85
	ds_read_b64_tr_b16 v[190:191], v206 offset:28672
	ds_read_b64_tr_b16 v[192:193], v206 offset:29184
	v_add_f32_e32 v82, v88, v130
	v_add_f32_e32 v82, v89, v82
	s_waitcnt lgkmcnt(10)
	v_mfma_f32_32x32x16_bf16 v[98:113], v[186:189], v[158:161], v[50:65]
	v_add_f32_e32 v82, v90, v82
	v_add_f32_e32 v82, v91, v82
	v_cvt_pk_bf16_f32 v144, v86, v87
	v_cvt_pk_bf16_f32 v145, v88, v89
	ds_read_b64_tr_b16 v[186:187], v206 offset:25600
	ds_read_b64_tr_b16 v[188:189], v206 offset:26112
	s_waitcnt lgkmcnt(11)
	v_mfma_f32_32x32x16_bf16 v[114:129], v[182:185], v[154:157], v[114:129]
	v_add_f32_e32 v82, v92, v82
	v_add_f32_e32 v82, v93, v82
	v_add_f32_e32 v82, v94, v82
	v_add_f32_e32 v82, v95, v82
	v_cvt_pk_bf16_f32 v138, v90, v91
	v_cvt_pk_bf16_f32 v139, v92, v93
	ds_read_b64_tr_b16 v[86:87], v206 offset:29696
	ds_read_b64_tr_b16 v[88:89], v206 offset:30208
	s_waitcnt lgkmcnt(12)
	v_mfma_f32_32x32x16_bf16 v[98:113], v[178:181], v[154:157], v[98:113]
	v_add_f32_e32 v82, v96, v82
	v_add_f32_e32 v82, v97, v82
	v_add_f32_e32 v82, v66, v82
	v_add_f32_e32 v90, v67, v82
	v_cvt_pk_bf16_f32 v140, v94, v95
	v_cvt_pk_bf16_f32 v141, v96, v97
	ds_read_b64_tr_b16 v[82:83], v206 offset:26624
	ds_read_b64_tr_b16 v[84:85], v206 offset:27136
	s_waitcnt lgkmcnt(13)
	v_mfma_f32_32x32x16_bf16 v[114:129], v[174:177], v[150:153], v[114:129]
	v_add_f32_e32 v90, v68, v90
	v_add_f32_e32 v90, v69, v90
	v_add_f32_e32 v90, v70, v90
	v_add_f32_e32 v90, v71, v90
	v_cvt_pk_bf16_f32 v134, v66, v67
	v_cvt_pk_bf16_f32 v135, v68, v69
	ds_read_b64_tr_b16 v[66:67], v206 offset:30720
	ds_read_b64_tr_b16 v[68:69], v206 offset:31232
	s_waitcnt lgkmcnt(14)
	v_mfma_f32_32x32x16_bf16 v[98:113], v[170:173], v[150:153], v[98:113]
	v_add_f32_e32 v90, v72, v90
	v_add_f32_e32 v90, v73, v90
	v_add_f32_e32 v90, v74, v90
	v_add_f32_e32 v90, v75, v90
	v_cvt_pk_bf16_f32 v136, v70, v71
	v_cvt_pk_bf16_f32 v137, v72, v73
	ds_read_b64_tr_b16 v[70:71], v206 offset:27648
	ds_read_b64_tr_b16 v[72:73], v206 offset:28160
	s_waitcnt lgkmcnt(14)
	v_mfma_f32_32x32x16_bf16 v[114:129], v[166:169], v[146:149], v[114:129]
	v_add_f32_e32 v90, v76, v90
	v_add_f32_e32 v90, v77, v90
	v_add_f32_e32 v90, v78, v90
	v_add_f32_e32 v90, v79, v90
	v_cvt_pk_bf16_f32 v130, v74, v75
	v_cvt_pk_bf16_f32 v131, v76, v77
	ds_read_b64_tr_b16 v[74:75], v206 offset:31744
	ds_read_b64_tr_b16 v[76:77], v206 offset:32256
	v_mfma_f32_32x32x16_bf16 v[98:113], v[162:165], v[146:149], v[98:113]
	v_add_f32_e32 v90, v80, v90
	v_add_f32_e32 v90, v81, v90
	v_cvt_pk_bf16_f32 v132, v78, v79
	v_cvt_pk_bf16_f32 v133, v80, v81
	s_nop 0
	v_lshl_add_u64 v[78:79], v[204:205], 0, s[24:25]
	s_add_i32 s26, s39, s35
	s_mov_b32 m0, s26
	s_nop 0
	global_load_lds_dwordx4 v[78:79], off
	v_max_f32_e32 v78, v114, v115
	s_nop 2
	v_max3_f32 v79, v116, v117, v99
	v_max3_f32 v78, v78, v98, v100
	v_max3_f32 v78, v78, v101, v118
	v_max3_f32 v79, v79, v120, v121
	v_max3_f32 v78, v78, v119, v102
	v_max3_f32 v79, v79, v104, v105
	v_max3_f32 v78, v78, v103, v122
	v_max3_f32 v79, v79, v124, v125
	v_max3_f32 v78, v78, v123, v106
	v_max3_f32 v79, v79, v108, v109
	v_max3_f32 v78, v78, v107, v126
	v_max3_f32 v79, v79, v128, v129
	v_max3_f32 v78, v78, v127, v110
	v_max3_f32 v79, v79, v112, v113
	v_max3_f32 v78, v78, v111, v79
	v_mov_b32_e32 v79, v78
	v_lshl_add_u64 v[206:207], v[208:209], 0, s[18:19]
	s_add_i32 s26, s38, s34
	v_permlane32_swap_b32_e32 v78, v79
	v_max_f32_e32 v78, v78, v79
	s_mov_b32 m0, s26
	s_nop 0
	global_load_lds_dwordx4 v[206:207], off
	v_cmp_lt_f32_e32 vcc, s15, v78
	s_cmp_lg_u64 vcc, 0
	v_add_f32_e32 v201, v201, v90
	s_cselect_b64 s[26:27], -1, 0
	s_cbranch_vccnz .LBB3_11

.LBB3_6:
	s_add_i32 s26, s38, 0x2000
	s_cmpk_lg_i32 s38, 0x4000
	s_cselect_b32 s40, s26, 0
	v_add_u32_e32 v217, s39, v214
	ds_read_b64_tr_b16 v[162:163], v217 offset:24576
	ds_read_b64_tr_b16 v[164:165], v217 offset:25088
	s_waitcnt lgkmcnt(9)
	v_mfma_f32_32x32x16_bf16 v[82:97], v[78:81], v[158:161], v[50:65]
	v_add_f32_e32 v66, v114, v115
	v_add_f32_e32 v66, v116, v66
	v_add_f32_e32 v66, v117, v66
	v_add_f32_e32 v66, v118, v66
	v_add_f32_e32 v66, v119, v66
	v_cvt_pk_bf16_f32 v142, v114, v115
	v_cvt_pk_bf16_f32 v143, v116, v117
	ds_read_b64_tr_b16 v[170:171], v217 offset:28672
	ds_read_b64_tr_b16 v[172:173], v217 offset:29184
	v_add_f32_e32 v66, v120, v66
	v_add_f32_e32 v66, v121, v66
	v_add_f32_e32 v66, v122, v66
	v_add_f32_e32 v114, v123, v66
	s_waitcnt lgkmcnt(10)
	v_mfma_f32_32x32x16_bf16 v[66:81], v[166:169], v[158:161], v[50:65]
	v_cvt_pk_bf16_f32 v144, v118, v119
	v_cvt_pk_bf16_f32 v145, v120, v121
	ds_read_b64_tr_b16 v[166:167], v217 offset:25600
	ds_read_b64_tr_b16 v[168:169], v217 offset:26112
	s_waitcnt lgkmcnt(11)
	v_mfma_f32_32x32x16_bf16 v[82:97], v[194:197], v[154:157], v[82:97]
	v_add_f32_e32 v114, v124, v114
	v_add_f32_e32 v114, v125, v114
	v_add_f32_e32 v114, v126, v114
	v_add_f32_e32 v114, v127, v114
	v_cvt_pk_bf16_f32 v138, v122, v123
	v_cvt_pk_bf16_f32 v139, v124, v125
	ds_read_b64_tr_b16 v[118:119], v217 offset:29696
	ds_read_b64_tr_b16 v[120:121], v217 offset:30208
	s_waitcnt lgkmcnt(12)
	v_mfma_f32_32x32x16_bf16 v[66:81], v[190:193], v[154:157], v[66:81]
	v_add_f32_e32 v114, v128, v114
	v_add_f32_e32 v114, v129, v114
	v_add_f32_e32 v114, v98, v114
	v_add_f32_e32 v122, v99, v114
	v_cvt_pk_bf16_f32 v140, v126, v127
	v_cvt_pk_bf16_f32 v141, v128, v129
	ds_read_b64_tr_b16 v[114:115], v217 offset:26624
	ds_read_b64_tr_b16 v[116:117], v217 offset:27136
	s_waitcnt lgkmcnt(13)
	v_mfma_f32_32x32x16_bf16 v[82:97], v[186:189], v[150:153], v[82:97]
	v_add_f32_e32 v122, v100, v122
	v_add_f32_e32 v122, v101, v122
	v_add_f32_e32 v122, v102, v122
	v_add_f32_e32 v122, v103, v122
	v_cvt_pk_bf16_f32 v134, v98, v99
	v_cvt_pk_bf16_f32 v135, v100, v101
	ds_read_b64_tr_b16 v[98:99], v217 offset:30720
	ds_read_b64_tr_b16 v[100:101], v217 offset:31232
	s_waitcnt lgkmcnt(14)
	v_mfma_f32_32x32x16_bf16 v[66:81], v[178:181], v[150:153], v[66:81]
	v_add_f32_e32 v122, v104, v122
	v_add_f32_e32 v122, v105, v122
	v_add_f32_e32 v122, v106, v122
	v_add_f32_e32 v122, v107, v122
	v_cvt_pk_bf16_f32 v136, v102, v103
	v_cvt_pk_bf16_f32 v137, v104, v105
	ds_read_b64_tr_b16 v[102:103], v217 offset:27648
	ds_read_b64_tr_b16 v[104:105], v217 offset:28160
	s_waitcnt lgkmcnt(14)
	v_mfma_f32_32x32x16_bf16 v[82:97], v[182:185], v[146:149], v[82:97]
	v_add_f32_e32 v122, v108, v122
	v_add_f32_e32 v122, v109, v122
	v_add_f32_e32 v122, v110, v122
	v_add_f32_e32 v122, v111, v122
	v_cvt_pk_bf16_f32 v130, v106, v107
	v_cvt_pk_bf16_f32 v131, v108, v109
	ds_read_b64_tr_b16 v[106:107], v217 offset:31744
	ds_read_b64_tr_b16 v[108:109], v217 offset:32256
	v_mfma_f32_32x32x16_bf16 v[66:81], v[174:177], v[146:149], v[66:81]
	v_add_f32_e32 v122, v112, v122
	v_add_f32_e32 v122, v113, v122
	v_cvt_pk_bf16_f32 v132, v110, v111
	v_cvt_pk_bf16_f32 v133, v112, v113
	s_nop 0
	v_lshl_add_u64 v[110:111], v[204:205], 0, s[20:21]
	s_add_i32 s26, s38, s35
	s_mov_b32 m0, s26
	s_nop 0
	global_load_lds_dwordx4 v[110:111], off
	v_lshl_add_u64 v[110:111], v[208:209], 0, s[16:17]
	s_add_i32 s26, s40, s34
	s_mov_b32 m0, s26
	s_nop 0
	global_load_lds_dwordx4 v[110:111], off
	v_max_f32_e32 v110, v82, v83
	s_nop 0
	v_max3_f32 v111, v84, v85, v67
	v_max3_f32 v110, v110, v66, v68
	v_max3_f32 v110, v110, v69, v86
	v_max3_f32 v111, v111, v88, v89
	v_max3_f32 v110, v110, v87, v70
	v_max3_f32 v111, v111, v72, v73
	v_max3_f32 v110, v110, v71, v90
	v_max3_f32 v111, v111, v92, v93
	v_max3_f32 v110, v110, v91, v74
	v_max3_f32 v111, v111, v76, v77
	v_max3_f32 v110, v110, v75, v94
	v_max3_f32 v111, v111, v96, v97
	v_max3_f32 v110, v110, v95, v78
	v_max3_f32 v111, v111, v80, v81
	v_max3_f32 v110, v110, v79, v111
	v_mov_b32_e32 v111, v110
	v_add_f32_e32 v201, v201, v122
	s_nop 0
	v_permlane32_swap_b32_e32 v110, v111
	v_max_f32_e32 v110, v110, v111
	v_cmp_lt_f32_e32 vcc, s15, v110
	s_cmp_lg_u64 vcc, 0
	s_cselect_b64 s[26:27], -1, 0
	s_cbranch_vccnz .LBB3_14
